# static priority raise for waves 4-7 from the start of DSA pass 1 through the attention loop; on top of v27
# baseline (speedup 1.0000x reference)
.LBB0_497:
	s_or_b64 exec, exec, s[0:1]
	s_mul_i32 s0, s44, 0x1200000
	s_mul_hi_i32 s1, s44, 0x1200000
	s_add_u32 s0, s74, s0
	s_addc_u32 s1, s75, s1
	s_add_i32 s12, 0, 0x23400
	v_ashrrev_i32_e32 v54, 4, v42
	v_mov_b32_e32 v0, s12
	s_lshl_b32 s49, s30, 6
	v_readlane_b32 s13, v252, 19
	v_and_b32_e32 v232, 15, v42
	s_waitcnt lgkmcnt(0)
	s_barrier
	ds_read_b128 v[6:9], v0
	ds_read_b128 v[2:5], v0 offset:16
	s_or_b32 s12, s49, s13
	v_mov_b32_e32 v0, v54
	v_or_b32_e32 v44, s12, v232
	v_mov_b64_e32 v[10:11], s[0:1]
	v_lshlrev_b32_e32 v12, 3, v0
	v_mad_i64_i32 v[10:11], s[0:1], v44, s2, v[10:11]
	v_ashrrev_i32_e32 v13, 31, v12
	v_lshl_add_u64 v[38:39], v[12:13], 1, v[10:11]
	global_load_dwordx4 v[10:13], v[38:39], off offset:2048
	global_load_dwordx4 v[14:17], v[38:39], off offset:2112
	v_ashrrev_i32_e32 v45, 31, v44
	v_lshlrev_b64 v[18:19], 9, v[44:45]
	v_lshl_add_u64 v[18:19], s[42:43], 0, v[18:19]
	global_load_dwordx2 v[50:51], v[18:19], off offset:384
	global_load_dwordx4 v[72:75], v[38:39], off offset:2048
	global_load_dwordx4 v[76:79], v[38:39], off offset:2112
	global_load_dwordx4 v[80:83], v[38:39], off offset:2176
	global_load_dwordx4 v[84:87], v[38:39], off offset:2240
	global_load_dwordx4 v[88:91], v[38:39], off offset:2304
	global_load_dwordx4 v[92:95], v[38:39], off offset:2368
	global_load_dwordx4 v[96:99], v[38:39], off offset:2432
	global_load_dwordx4 v[100:103], v[38:39], off offset:2496
	v_ashrrev_i32_e32 v233, 3, v42
	v_readlane_b32 s12, v251, 50
	s_add_u32 s0, s42, 0x100
	s_addc_u32 s1, s43, 0
	v_add_u32_e32 v46, s12, v233
	v_ashrrev_i32_e32 v47, 31, v46
	v_lshlrev_b64 v[46:47], 9, v[46:47]
	s_movk_i32 s12, 0x70
	s_mov_b64 s[16:17], 0x8000
	s_add_i32 s30, s30, 2
	s_ashr_i32 s50, s30, 1
	v_ashrrev_i32_e32 v43, 31, v42
	s_waitcnt vmcnt(2)
	v_lshlrev_b32_e32 v0, 16, v10
	v_and_b32_e32 v10, 0xffff0000, v10
	v_lshlrev_b32_e32 v18, 16, v11
	v_and_b32_e32 v11, 0xffff0000, v11
	v_lshlrev_b32_e32 v19, 16, v12
	v_and_b32_e32 v12, 0xffff0000, v12
	v_mul_f32_e32 v10, v10, v10
	v_mul_f32_e32 v11, v11, v11
	v_lshlrev_b32_e32 v20, 16, v13
	v_and_b32_e32 v13, 0xffff0000, v13
	v_mul_f32_e32 v12, v12, v12
	v_fmac_f32_e32 v10, v0, v0
	v_fmac_f32_e32 v11, v18, v18
	s_waitcnt vmcnt(1)
	v_lshlrev_b32_e32 v21, 16, v14
	v_and_b32_e32 v14, 0xffff0000, v14
	v_mul_f32_e32 v13, v13, v13
	v_fmac_f32_e32 v12, v19, v19
	v_add_f32_e32 v0, v10, v11
	v_lshlrev_b32_e32 v22, 16, v15
	v_and_b32_e32 v15, 0xffff0000, v15
	v_mul_f32_e32 v14, v14, v14
	v_fmac_f32_e32 v13, v20, v20
	v_add_f32_e32 v0, v12, v0
	v_lshlrev_b32_e32 v23, 16, v16
	v_and_b32_e32 v16, 0xffff0000, v16
	v_mul_f32_e32 v15, v15, v15
	v_fmac_f32_e32 v14, v21, v21
	v_add_f32_e32 v0, v13, v0
	v_lshlrev_b32_e32 v24, 16, v17
	v_and_b32_e32 v17, 0xffff0000, v17
	v_mul_f32_e32 v16, v16, v16
	v_fmac_f32_e32 v15, v22, v22
	v_add_f32_e32 v0, v14, v0
	v_mul_f32_e32 v17, v17, v17
	v_fmac_f32_e32 v16, v23, v23
	v_add_f32_e32 v0, v15, v0
	v_fmac_f32_e32 v17, v24, v24
	v_add_f32_e32 v0, v16, v0
	v_add_f32_e32 v0, v17, v0
	v_mov_b32_e32 v10, v0
	s_nop 1
	v_permlane16_swap_b32_e32 v0, v10
	v_add_f32_e32 v56, v0, v10
	v_mov_b32_e32 v57, v56
	v_mov_b64_e32 v[10:11], v[80:81]
	v_mov_b64_e32 v[12:13], v[82:83]
	v_mov_b64_e32 v[14:15], v[84:85]
	v_mov_b64_e32 v[16:17], v[86:87]
	v_permlane32_swap_b32_e32 v56, v57
	s_waitcnt vmcnt(1)
	v_lshlrev_b32_e32 v0, 16, v10
	v_and_b32_e32 v10, 0xffff0000, v10
	v_lshlrev_b32_e32 v18, 16, v11
	v_and_b32_e32 v11, 0xffff0000, v11
	v_lshlrev_b32_e32 v19, 16, v12
	v_and_b32_e32 v12, 0xffff0000, v12
	v_mul_f32_e32 v10, v10, v10
	v_mul_f32_e32 v11, v11, v11
	v_lshlrev_b32_e32 v20, 16, v13
	v_and_b32_e32 v13, 0xffff0000, v13
	v_mul_f32_e32 v12, v12, v12
	v_fmac_f32_e32 v10, v0, v0
	v_fmac_f32_e32 v11, v18, v18
	s_waitcnt vmcnt(0)
	v_lshlrev_b32_e32 v21, 16, v14
	v_and_b32_e32 v14, 0xffff0000, v14
	v_mul_f32_e32 v13, v13, v13
	v_fmac_f32_e32 v12, v19, v19
	v_add_f32_e32 v0, v10, v11
	v_lshlrev_b32_e32 v22, 16, v15
	v_and_b32_e32 v15, 0xffff0000, v15
	v_mul_f32_e32 v14, v14, v14
	v_fmac_f32_e32 v13, v20, v20
	v_add_f32_e32 v0, v12, v0
	v_lshlrev_b32_e32 v23, 16, v16
	v_and_b32_e32 v16, 0xffff0000, v16
	v_mul_f32_e32 v15, v15, v15
	v_fmac_f32_e32 v14, v21, v21
	v_add_f32_e32 v0, v13, v0
	v_lshlrev_b32_e32 v24, 16, v17
	v_and_b32_e32 v17, 0xffff0000, v17
	v_mul_f32_e32 v16, v16, v16
	v_fmac_f32_e32 v15, v22, v22
	v_add_f32_e32 v0, v14, v0
	v_mul_f32_e32 v17, v17, v17
	v_fmac_f32_e32 v16, v23, v23
	v_add_f32_e32 v0, v15, v0
	v_fmac_f32_e32 v17, v24, v24
	v_add_f32_e32 v0, v16, v0
	v_add_f32_e32 v0, v17, v0
	v_mov_b32_e32 v10, v0
	s_nop 1
	v_permlane16_swap_b32_e32 v0, v10
	v_add_f32_e32 v58, v0, v10
	v_mov_b32_e32 v59, v58
	v_mov_b64_e32 v[10:11], v[88:89]
	v_mov_b64_e32 v[12:13], v[90:91]
	v_mov_b64_e32 v[14:15], v[92:93]
	v_mov_b64_e32 v[16:17], v[94:95]
	v_permlane32_swap_b32_e32 v58, v59
	s_waitcnt vmcnt(1)
	v_lshlrev_b32_e32 v0, 16, v10
	v_and_b32_e32 v10, 0xffff0000, v10
	v_lshlrev_b32_e32 v18, 16, v11
	v_and_b32_e32 v11, 0xffff0000, v11
	v_lshlrev_b32_e32 v19, 16, v12
	v_and_b32_e32 v12, 0xffff0000, v12
	v_mul_f32_e32 v10, v10, v10
	v_mul_f32_e32 v11, v11, v11
	v_lshlrev_b32_e32 v20, 16, v13
	v_and_b32_e32 v13, 0xffff0000, v13
	v_mul_f32_e32 v12, v12, v12
	v_fmac_f32_e32 v10, v0, v0
	v_fmac_f32_e32 v11, v18, v18
	s_waitcnt vmcnt(0)
	v_lshlrev_b32_e32 v21, 16, v14
	v_and_b32_e32 v14, 0xffff0000, v14
	v_mul_f32_e32 v13, v13, v13
	v_fmac_f32_e32 v12, v19, v19
	v_add_f32_e32 v0, v10, v11
	v_lshlrev_b32_e32 v22, 16, v15
	v_and_b32_e32 v15, 0xffff0000, v15
	v_mul_f32_e32 v14, v14, v14
	v_fmac_f32_e32 v13, v20, v20
	v_add_f32_e32 v0, v12, v0
	v_lshlrev_b32_e32 v23, 16, v16
	v_and_b32_e32 v16, 0xffff0000, v16
	v_mul_f32_e32 v15, v15, v15
	v_fmac_f32_e32 v14, v21, v21
	v_add_f32_e32 v0, v13, v0
	v_lshlrev_b32_e32 v24, 16, v17
	v_and_b32_e32 v17, 0xffff0000, v17
	v_mul_f32_e32 v16, v16, v16
	v_fmac_f32_e32 v15, v22, v22
	v_add_f32_e32 v0, v14, v0
	v_mul_f32_e32 v17, v17, v17
	v_fmac_f32_e32 v16, v23, v23
	v_add_f32_e32 v0, v15, v0
	v_fmac_f32_e32 v17, v24, v24
	v_add_f32_e32 v0, v16, v0
	v_add_f32_e32 v0, v17, v0
	v_mov_b32_e32 v10, v0
	s_nop 1
	v_permlane16_swap_b32_e32 v0, v10
	v_add_f32_e32 v60, v0, v10
	v_mov_b32_e32 v61, v60
	v_mov_b64_e32 v[10:11], v[96:97]
	v_mov_b64_e32 v[12:13], v[98:99]
	v_mov_b64_e32 v[14:15], v[100:101]
	v_mov_b64_e32 v[16:17], v[102:103]
	v_permlane32_swap_b32_e32 v60, v61
	s_waitcnt vmcnt(1)
	v_lshlrev_b32_e32 v0, 16, v10
	v_and_b32_e32 v10, 0xffff0000, v10
	v_lshlrev_b32_e32 v18, 16, v11
	v_and_b32_e32 v11, 0xffff0000, v11
	v_lshlrev_b32_e32 v19, 16, v12
	v_and_b32_e32 v12, 0xffff0000, v12
	v_mul_f32_e32 v10, v10, v10
	v_mul_f32_e32 v11, v11, v11
	v_lshlrev_b32_e32 v20, 16, v13
	v_and_b32_e32 v13, 0xffff0000, v13
	v_mul_f32_e32 v12, v12, v12
	v_fmac_f32_e32 v10, v0, v0
	v_fmac_f32_e32 v11, v18, v18
	s_waitcnt vmcnt(0)
	v_lshlrev_b32_e32 v21, 16, v14
	v_and_b32_e32 v14, 0xffff0000, v14
	v_mul_f32_e32 v13, v13, v13
	v_fmac_f32_e32 v12, v19, v19
	v_add_f32_e32 v0, v10, v11
	v_lshlrev_b32_e32 v22, 16, v15
	v_and_b32_e32 v15, 0xffff0000, v15
	v_mul_f32_e32 v14, v14, v14
	v_fmac_f32_e32 v13, v20, v20
	v_add_f32_e32 v0, v12, v0
	v_lshlrev_b32_e32 v23, 16, v16
	v_and_b32_e32 v16, 0xffff0000, v16
	v_mul_f32_e32 v15, v15, v15
	v_fmac_f32_e32 v14, v21, v21
	v_add_f32_e32 v0, v13, v0
	v_lshlrev_b32_e32 v24, 16, v17
	v_and_b32_e32 v17, 0xffff0000, v17
	v_mul_f32_e32 v16, v16, v16
	v_fmac_f32_e32 v15, v22, v22
	v_add_f32_e32 v0, v14, v0
	v_mul_f32_e32 v17, v17, v17
	v_fmac_f32_e32 v16, v23, v23
	v_add_f32_e32 v0, v15, v0
	v_fmac_f32_e32 v17, v24, v24
	v_add_f32_e32 v0, v16, v0
	v_add_f32_e32 v0, v17, v0
	v_mov_b32_e32 v10, v0
	s_nop 1
	v_permlane16_swap_b32_e32 v0, v10
	v_add_f32_e32 v62, v0, v10
	v_mov_b32_e32 v63, v62
	v_mov_b64_e32 v[30:31], v[72:73]
	v_mov_b64_e32 v[32:33], v[74:75]
	v_mov_b64_e32 v[26:27], v[76:77]
	v_mov_b64_e32 v[28:29], v[78:79]
	v_mov_b64_e32 v[22:23], v[80:81]
	v_mov_b64_e32 v[24:25], v[82:83]
	v_mov_b64_e32 v[18:19], v[84:85]
	v_mov_b64_e32 v[20:21], v[86:87]
	v_mov_b64_e32 v[14:15], v[88:89]
	v_mov_b64_e32 v[16:17], v[90:91]
	v_mov_b64_e32 v[10:11], v[92:93]
	v_mov_b64_e32 v[12:13], v[94:95]
	v_mov_b64_e32 v[34:35], v[96:97]
	v_mov_b64_e32 v[36:37], v[98:99]
	s_nop 0
	v_mov_b64_e32 v[38:39], v[100:101]
	v_mov_b64_e32 v[40:41], v[102:103]
	v_xor_b32_e32 v0, v233, v42
	v_lshlrev_b32_e32 v0, 4, v0
	v_and_or_b32 v46, v0, s12, v46
	v_lshl_add_u64 v[48:49], v[46:47], 0, s[16:17]
	v_lshl_add_u64 v[64:65], s[0:1], 0, v[46:47]
	s_mov_b32 s12, m0
	s_mov_b32 m0, s93
	s_nop 0
	global_load_lds_dwordx4 v[64:65], off
	s_mov_b32 m0, s12
	v_lshl_add_u64 v[64:65], s[0:1], 0, v[48:49]
	s_add_i32 s0, s93, 0x2000
	s_mov_b32 s1, m0
	s_mov_b32 m0, s0
	s_nop 0
	global_load_lds_dwordx4 v[64:65], off
	s_mov_b32 m0, s1
	s_cmp_gt_i32 s50, 0
	v_permlane32_swap_b32_e32 v62, v63
	s_cselect_b64 s[46:47], -1, 0
	s_cmp_lt_i32 s50, 1
	v_or_b32_e32 v0, s13, v232
	s_cbranch_scc1 .LBB0_510
	s_waitcnt lgkmcnt(1)
	v_mov_b32_e32 v64, v6
	s_waitcnt lgkmcnt(0)
	v_mov_b32_e32 v65, v2
	v_mov_b32_e32 v2, v7
	v_mov_b32_e32 v6, v8
	v_mov_b32_e32 v7, v4
	v_mov_b32_e32 v4, v9
	v_pk_add_f32 v[2:3], v[64:65], v[2:3]
	v_pk_add_f32 v[4:5], v[6:7], v[4:5]
	v_lshlrev_b32_e32 v45, 16, v50
	v_pk_add_f32 v[2:3], v[2:3], v[4:5]
	v_mul_f32_e32 v66, 0x3d800000, v45
	v_add_f32_e32 v2, v2, v3
	v_mul_f32_e32 v2, 0x39000000, v2
	v_mul_f32_e32 v3, 0x4f800000, v2
	v_cmp_gt_f32_e64 s[0:1], s78, v2
	v_and_b32_e32 v45, 0xffff0000, v50
	v_mul_f32_e32 v67, 0x3d800000, v45
	v_cndmask_b32_e64 v2, v2, v3, s[0:1]
	v_sqrt_f32_e32 v3, v2
	s_mov_b32 s12, 0x40400000
	v_cmp_lt_f32_e64 s[30:31], 0, v66
	v_cmp_lt_f32_e32 vcc, 0, v67
	v_add_u32_e32 v4, -1, v3
	v_fma_f32 v5, -v4, v3, v2
	v_cmp_ge_f32_e64 s[40:41], 0, v5
	v_add_u32_e32 v5, 1, v3
	v_lshlrev_b32_e32 v45, 16, v51
	v_cndmask_b32_e64 v4, v3, v4, s[40:41]
	v_fma_f32 v3, -v5, v3, v2
	v_cmp_lt_f32_e64 s[40:41], 0, v3
	v_mul_f32_e32 v68, 0x3d800000, v45
	v_cmp_lt_f32_e64 s[34:35], 0, v68
	v_cndmask_b32_e64 v3, v4, v5, s[40:41]
	v_add_f32_e32 v5, v56, v57
	v_mul_f32_e32 v6, 0x4f800000, v5
	v_cmp_gt_f32_e64 s[40:41], s78, v5
	v_mul_f32_e32 v4, 0x37800000, v3
	v_cndmask_b32_e64 v3, v3, v4, s[0:1]
	v_cndmask_b32_e64 v5, v5, v6, s[40:41]
	v_sqrt_f32_e32 v6, v5
	v_cmp_class_f32_e64 s[0:1], v2, v231
	v_and_b32_e32 v45, 0xffff0000, v51
	v_mul_f32_e32 v69, 0x3d800000, v45
	v_cndmask_b32_e64 v2, v3, v2, s[0:1]
	v_add_u32_e32 v3, -1, v6
	v_fma_f32 v4, -v3, v6, v5
	v_cmp_ge_f32_e64 s[0:1], 0, v4
	v_add_u32_e32 v4, 1, v6
	v_cmp_lt_f32_e64 s[36:37], 0, v69
	v_cndmask_b32_e64 v3, v6, v3, s[0:1]
	v_fma_f32 v6, -v4, v6, v5
	v_cmp_lt_f32_e64 s[0:1], 0, v6
	v_mov_b32_e32 v55, 0xff800000
	v_mov_b32_e32 v70, 0x7f800000
	v_cndmask_b32_e64 v3, v3, v4, s[0:1]
	v_mul_f32_e32 v4, 0x37800000, v3
	v_cndmask_b32_e64 v3, v3, v4, s[40:41]
	v_cmp_class_f32_e64 s[0:1], v5, v231
	v_add_f32_e32 v4, v58, v59
	v_cndmask_b32_e64 v51, v55, 0, vcc
	v_cndmask_b32_e64 v3, v3, v5, s[0:1]
	v_mul_f32_e32 v5, 0x4f800000, v4
	v_cmp_gt_f32_e64 s[0:1], s78, v4
	v_mul_f32_e64 v3, |v66|, v3
	v_mul_f32_e32 v3, v2, v3
	v_cndmask_b32_e64 v4, v4, v5, s[0:1]
	v_sqrt_f32_e32 v5, v4
	v_fma_f32 v3, v3, s12, 0
	v_cndmask_b32_e64 v6, 0, v3, s[30:31]
	v_cndmask_b32_e64 v3, v3, 0, s[30:31]
	v_add_u32_e32 v7, -1, v5
	v_fma_f32 v8, -v7, v5, v4
	v_cmp_ge_f32_e64 s[40:41], 0, v8
	v_add_u32_e32 v8, 1, v5
	s_mov_b32 s12, 0x467c0400
	v_cndmask_b32_e64 v7, v5, v7, s[40:41]
	v_fma_f32 v5, -v8, v5, v4
	v_cmp_lt_f32_e64 s[40:41], 0, v5
	v_cndmask_b32_e64 v45, v55, 0, s[30:31]
	v_cndmask_b32_e64 v50, 0, v70, s[30:31]
	v_cndmask_b32_e64 v5, v7, v8, s[40:41]
	v_mul_f32_e32 v7, 0x37800000, v5
	v_cndmask_b32_e64 v5, v5, v7, s[0:1]
	v_cmp_class_f32_e64 s[0:1], v4, v231
	v_readlane_b32 s30, v251, 39
	v_cndmask_b32_e64 v53, v55, 0, s[34:35]
	v_cndmask_b32_e64 v4, v5, v4, s[0:1]
	v_add_f32_e32 v5, v60, v61
	v_mul_f32_e32 v7, 0x4f800000, v5
	v_cmp_gt_f32_e64 s[0:1], s78, v5
	v_mul_f32_e64 v4, |v67|, v4
	v_mul_f32_e32 v4, v2, v4
	v_cndmask_b32_e64 v5, v5, v7, s[0:1]
	v_sqrt_f32_e32 v7, v5
	v_fmamk_f32 v8, v4, 0x40400000, v6
	v_cndmask_b32_e32 v6, v6, v8, vcc
	v_fmamk_f32 v4, v4, 0x40400000, v3
	v_add_u32_e32 v8, -1, v7
	v_fma_f32 v9, -v8, v7, v5
	v_cmp_ge_f32_e64 s[40:41], 0, v9
	v_add_u32_e32 v9, 1, v7
	v_cndmask_b32_e32 v3, v4, v3, vcc
	v_cndmask_b32_e64 v8, v7, v8, s[40:41]
	v_fma_f32 v7, -v9, v7, v5
	v_cmp_lt_f32_e64 s[40:41], 0, v7
	v_cndmask_b32_e64 v55, v55, 0, s[36:37]
	v_cndmask_b32_e64 v57, 0, v70, s[34:35]
	v_cndmask_b32_e64 v7, v8, v9, s[40:41]
	v_mul_f32_e32 v8, 0x37800000, v7
	v_cndmask_b32_e64 v7, v7, v8, s[0:1]
	v_cmp_class_f32_e64 s[0:1], v5, v231
	v_cndmask_b32_e64 v58, 0, v70, s[36:37]
	s_mov_b32 s13, 0
	v_cndmask_b32_e64 v5, v7, v5, s[0:1]
	v_add_f32_e32 v7, v62, v63
	v_mul_f32_e32 v8, 0x4f800000, v7
	v_cmp_gt_f32_e64 s[0:1], s78, v7
	v_mul_f32_e64 v5, |v68|, v5
	v_mul_f32_e32 v5, v2, v5
	v_cndmask_b32_e64 v7, v7, v8, s[0:1]
	v_sqrt_f32_e32 v8, v7
	v_fmamk_f32 v9, v5, 0x40400000, v6
	v_cndmask_b32_e64 v6, v6, v9, s[34:35]
	v_fmamk_f32 v4, v5, 0x40400000, v3
	v_add_u32_e32 v9, -1, v8
	v_fma_f32 v56, -v9, v8, v7
	v_cmp_ge_f32_e64 s[40:41], 0, v56
	v_add_u32_e32 v56, 1, v8
	v_cndmask_b32_e64 v3, v4, v3, s[34:35]
	v_cndmask_b32_e64 v9, v8, v9, s[40:41]
	v_fma_f32 v8, -v56, v8, v7
	v_cmp_lt_f32_e64 s[40:41], 0, v8
	s_nop 1
	v_cndmask_b32_e64 v8, v9, v56, s[40:41]
	v_mul_f32_e32 v9, 0x37800000, v8
	v_cndmask_b32_e64 v8, v8, v9, s[0:1]
	v_cmp_class_f32_e64 s[0:1], v7, v231
	v_cndmask_b32_e32 v56, 0, v70, vcc
	s_waitcnt vmcnt(0)
	v_and_b32_e32 v9, 0xffff0000, v41
	v_cndmask_b32_e64 v7, v8, v7, s[0:1]
	v_mul_f32_e64 v7, |v69|, v7
	v_mul_f32_e32 v2, v2, v7
	v_fmamk_f32 v7, v2, 0x40400000, v6
	v_fmamk_f32 v2, v2, 0x40400000, v3
	v_cndmask_b32_e64 v6, v6, v7, s[36:37]
	v_cndmask_b32_e64 v2, v2, v3, s[36:37]
	v_max_f32_e32 v2, v6, v2
	v_div_scale_f32 v3, s[0:1], v2, v2, s12
	v_rcp_f32_e32 v4, v3
	v_and_b32_e32 v8, 0xffff0000, v40
	s_movk_i32 s0, 0x70
	v_readlane_b32 s1, v253, 42
	v_fma_f32 v5, -v3, v4, 1.0
	v_fmac_f32_e32 v4, v5, v4
	v_div_scale_f32 v5, vcc, s12, v2, s12
	v_mul_f32_e32 v6, v5, v4
	v_fma_f32 v7, -v3, v6, v5
	v_fmac_f32_e32 v6, v7, v4
	v_fma_f32 v3, -v3, v6, v5
	v_div_fmas_f32 v3, v3, v4, v6
	v_div_fixup_f32 v3, v3, v2, s12
	v_cmp_lt_f32_e32 vcc, 0, v2
	v_and_b32_e32 v2, 0xffff0000, v38
	v_lshlrev_b32_e32 v5, 16, v39
	v_cndmask_b32_e32 v59, 0, v3, vcc
	v_mul_f32_e32 v6, v69, v59
	v_and_b32_e32 v3, 0xffff0000, v39
	v_pk_mul_f32 v[2:3], v[6:7], v[2:3] op_sel_hi:[0,1]
	v_lshlrev_b32_e32 v4, 16, v38
	v_pk_mul_f32 v[8:9], v[6:7], v[8:9] op_sel_hi:[0,1]
	v_lshlrev_b32_e32 v39, 16, v41
	v_lshlrev_b32_e32 v38, 16, v40
	v_pk_mul_f32 v[4:5], v[6:7], v[4:5] op_sel_hi:[0,1]
	v_pk_mul_f32 v[38:39], v[6:7], v[38:39] op_sel_hi:[0,1]
	v_bfe_u32 v7, v9, 16, 1
	v_bfe_u32 v41, v3, 16, 1
	v_bfe_u32 v40, v8, 16, 1
	v_bfe_u32 v60, v2, 16, 1
	v_add3_u32 v3, v3, v41, s39
	v_add3_u32 v7, v9, v7, s39
	v_bfe_u32 v9, v4, 16, 1
	v_bfe_u32 v41, v38, 16, 1
	v_add3_u32 v2, v2, v60, s39
	v_add3_u32 v8, v8, v40, s39
	v_bfe_u32 v40, v5, 16, 1
	v_bfe_u32 v60, v39, 16, 1
	v_add3_u32 v38, v38, v41, s39
	v_add3_u32 v4, v4, v9, s39
	v_add3_u32 v39, v39, v60, s39
	v_add3_u32 v5, v5, v40, s39
	v_lshrrev_b32_e32 v9, 16, v4
	v_lshrrev_b32_e32 v4, 16, v38
	v_lshrrev_b32_e32 v40, 16, v5
	v_lshrrev_b32_e32 v5, 16, v39
	v_and_or_b32 v4, v8, s38, v4
	v_and_or_b32 v2, v2, s38, v9
	v_and_b32_e32 v9, 0xffff0000, v35
	v_and_b32_e32 v8, 0xffff0000, v34
	v_and_b32_e32 v39, 0xffff0000, v37
	v_and_b32_e32 v38, 0xffff0000, v36
	v_pk_mul_f32 v[8:9], v[6:7], v[8:9] op_sel_hi:[0,1]
	v_lshlrev_b32_e32 v35, 16, v35
	v_lshlrev_b32_e32 v34, 16, v34
	v_pk_mul_f32 v[38:39], v[6:7], v[38:39] op_sel_hi:[0,1]
	v_lshlrev_b32_e32 v37, 16, v37
	v_lshlrev_b32_e32 v36, 16, v36
	v_and_or_b32 v5, v7, s38, v5
	v_and_or_b32 v3, v3, s38, v40
	v_pk_mul_f32 v[34:35], v[6:7], v[34:35] op_sel_hi:[0,1]
	v_pk_mul_f32 v[6:7], v[6:7], v[36:37] op_sel_hi:[0,1]
	v_bfe_u32 v36, v39, 16, 1
	v_bfe_u32 v37, v38, 16, 1
	v_bfe_u32 v40, v9, 16, 1
	v_bfe_u32 v41, v8, 16, 1
	v_add3_u32 v41, v8, v41, s39
	v_add3_u32 v40, v9, v40, s39
	v_add3_u32 v8, v38, v37, s39
	v_add3_u32 v9, v39, v36, s39
	v_bfe_u32 v36, v34, 16, 1
	v_bfe_u32 v38, v6, 16, 1
	v_bfe_u32 v37, v35, 16, 1
	v_add3_u32 v6, v6, v38, s39
	v_add3_u32 v34, v34, v36, s39
	v_bfe_u32 v39, v7, 16, 1
	v_add3_u32 v35, v35, v37, s39
	v_lshrrev_b32_e32 v34, 16, v34
	v_lshrrev_b32_e32 v6, 16, v6
	v_add3_u32 v7, v7, v39, s39
	v_lshrrev_b32_e32 v35, 16, v35
	v_and_or_b32 v8, v8, s38, v6
	v_and_or_b32 v6, v41, s38, v34
	v_mul_f32_e32 v34, v68, v59
	v_and_b32_e32 v37, 0xffff0000, v11
	v_and_b32_e32 v36, 0xffff0000, v10
	v_and_b32_e32 v39, 0xffff0000, v13
	v_and_b32_e32 v38, 0xffff0000, v12
	v_lshrrev_b32_e32 v7, 16, v7
	v_pk_mul_f32 v[36:37], v[34:35], v[36:37] op_sel_hi:[0,1]
	v_lshlrev_b32_e32 v11, 16, v11
	v_lshlrev_b32_e32 v10, 16, v10
	v_pk_mul_f32 v[38:39], v[34:35], v[38:39] op_sel_hi:[0,1]
	v_lshlrev_b32_e32 v13, 16, v13
	v_lshlrev_b32_e32 v12, 16, v12
	v_and_or_b32 v9, v9, s38, v7
	v_and_or_b32 v7, v40, s38, v35
	v_pk_mul_f32 v[10:11], v[34:35], v[10:11] op_sel_hi:[0,1]
	v_pk_mul_f32 v[12:13], v[34:35], v[12:13] op_sel_hi:[0,1]
	v_bfe_u32 v35, v39, 16, 1
	v_bfe_u32 v40, v38, 16, 1
	v_bfe_u32 v41, v37, 16, 1
	v_add3_u32 v37, v37, v41, s39
	v_add3_u32 v38, v38, v40, s39
	v_add3_u32 v35, v39, v35, s39
	v_bfe_u32 v39, v10, 16, 1
	v_bfe_u32 v40, v11, 16, 1
	v_bfe_u32 v41, v12, 16, 1
	v_bfe_u32 v60, v36, 16, 1
	v_add3_u32 v12, v12, v41, s39
	v_add3_u32 v11, v11, v40, s39
	v_add3_u32 v10, v10, v39, s39
	v_add3_u32 v36, v36, v60, s39
	v_bfe_u32 v60, v13, 16, 1
	v_lshrrev_b32_e32 v10, 16, v10
	v_lshrrev_b32_e32 v11, 16, v11
	v_lshrrev_b32_e32 v12, 16, v12
	v_add3_u32 v13, v13, v60, s39
	v_and_or_b32 v12, v38, s38, v12
	v_and_or_b32 v11, v37, s38, v11
	v_and_or_b32 v10, v36, s38, v10
	v_and_b32_e32 v37, 0xffff0000, v15
	v_and_b32_e32 v36, 0xffff0000, v14
	v_and_b32_e32 v39, 0xffff0000, v17
	v_and_b32_e32 v38, 0xffff0000, v16
	v_lshrrev_b32_e32 v13, 16, v13
	v_pk_mul_f32 v[36:37], v[34:35], v[36:37] op_sel_hi:[0,1]
	v_lshlrev_b32_e32 v15, 16, v15
	v_lshlrev_b32_e32 v14, 16, v14
	v_pk_mul_f32 v[38:39], v[34:35], v[38:39] op_sel_hi:[0,1]
	v_lshlrev_b32_e32 v17, 16, v17
	v_lshlrev_b32_e32 v16, 16, v16
	v_and_or_b32 v13, v35, s38, v13
	v_pk_mul_f32 v[14:15], v[34:35], v[14:15] op_sel_hi:[0,1]
	v_pk_mul_f32 v[16:17], v[34:35], v[16:17] op_sel_hi:[0,1]
	v_bfe_u32 v34, v39, 16, 1
	v_bfe_u32 v35, v38, 16, 1
	v_bfe_u32 v41, v36, 16, 1
	v_add3_u32 v36, v36, v41, s39
	v_add3_u32 v35, v38, v35, s39
	v_add3_u32 v34, v39, v34, s39
	v_bfe_u32 v38, v14, 16, 1
	v_bfe_u32 v39, v15, 16, 1
	v_bfe_u32 v41, v17, 16, 1
	v_bfe_u32 v40, v37, 16, 1
	v_add3_u32 v17, v17, v41, s39
	v_add3_u32 v15, v15, v39, s39
	v_add3_u32 v14, v14, v38, s39
	v_add3_u32 v37, v37, v40, s39
	v_bfe_u32 v40, v16, 16, 1
	v_lshrrev_b32_e32 v14, 16, v14
	v_lshrrev_b32_e32 v15, 16, v15
	v_lshrrev_b32_e32 v17, 16, v17
	v_add3_u32 v16, v16, v40, s39
	v_and_or_b32 v17, v34, s38, v17
	v_and_or_b32 v15, v37, s38, v15
	v_and_or_b32 v14, v36, s38, v14
	v_mul_f32_e32 v34, v67, v59
	v_and_b32_e32 v37, 0xffff0000, v19
	v_and_b32_e32 v36, 0xffff0000, v18
	v_and_b32_e32 v39, 0xffff0000, v21
	v_and_b32_e32 v38, 0xffff0000, v20
	v_lshrrev_b32_e32 v16, 16, v16
	v_pk_mul_f32 v[36:37], v[34:35], v[36:37] op_sel_hi:[0,1]
	v_lshlrev_b32_e32 v19, 16, v19
	v_lshlrev_b32_e32 v18, 16, v18
	v_pk_mul_f32 v[38:39], v[34:35], v[38:39] op_sel_hi:[0,1]
	v_lshlrev_b32_e32 v21, 16, v21
	v_lshlrev_b32_e32 v20, 16, v20
	v_and_or_b32 v16, v35, s38, v16
	v_pk_mul_f32 v[18:19], v[34:35], v[18:19] op_sel_hi:[0,1]
	v_pk_mul_f32 v[20:21], v[34:35], v[20:21] op_sel_hi:[0,1]
	v_bfe_u32 v35, v39, 16, 1
	v_bfe_u32 v40, v38, 16, 1
	v_bfe_u32 v41, v37, 16, 1
	v_add3_u32 v37, v37, v41, s39
	v_add3_u32 v38, v38, v40, s39
	v_add3_u32 v35, v39, v35, s39
	v_bfe_u32 v39, v18, 16, 1
	v_bfe_u32 v40, v19, 16, 1
	v_bfe_u32 v41, v20, 16, 1
	v_bfe_u32 v60, v36, 16, 1
	v_add3_u32 v20, v20, v41, s39
	v_add3_u32 v19, v19, v40, s39
	v_add3_u32 v18, v18, v39, s39
	v_add3_u32 v36, v36, v60, s39
	v_bfe_u32 v60, v21, 16, 1
	v_lshrrev_b32_e32 v18, 16, v18
	v_lshrrev_b32_e32 v19, 16, v19
	v_lshrrev_b32_e32 v20, 16, v20
	v_add3_u32 v21, v21, v60, s39
	v_and_or_b32 v20, v38, s38, v20
	v_and_or_b32 v19, v37, s38, v19
	v_and_or_b32 v18, v36, s38, v18
	v_and_b32_e32 v37, 0xffff0000, v23
	v_and_b32_e32 v36, 0xffff0000, v22
	v_and_b32_e32 v39, 0xffff0000, v25
	v_and_b32_e32 v38, 0xffff0000, v24
	v_lshrrev_b32_e32 v21, 16, v21
	v_pk_mul_f32 v[36:37], v[34:35], v[36:37] op_sel_hi:[0,1]
	v_lshlrev_b32_e32 v23, 16, v23
	v_lshlrev_b32_e32 v22, 16, v22
	v_pk_mul_f32 v[38:39], v[34:35], v[38:39] op_sel_hi:[0,1]
	v_lshlrev_b32_e32 v25, 16, v25
	v_lshlrev_b32_e32 v24, 16, v24
	v_and_or_b32 v21, v35, s38, v21
	v_pk_mul_f32 v[22:23], v[34:35], v[22:23] op_sel_hi:[0,1]
	v_pk_mul_f32 v[24:25], v[34:35], v[24:25] op_sel_hi:[0,1]
	v_bfe_u32 v34, v39, 16, 1
	v_bfe_u32 v35, v38, 16, 1
	v_bfe_u32 v41, v36, 16, 1
	v_add3_u32 v36, v36, v41, s39
	v_add3_u32 v35, v38, v35, s39
	v_add3_u32 v34, v39, v34, s39
	v_bfe_u32 v38, v22, 16, 1
	v_bfe_u32 v39, v23, 16, 1
	v_bfe_u32 v41, v25, 16, 1
	v_bfe_u32 v40, v37, 16, 1
	v_add3_u32 v25, v25, v41, s39
	v_add3_u32 v23, v23, v39, s39
	v_add3_u32 v22, v22, v38, s39
	v_add3_u32 v37, v37, v40, s39
	v_lshrrev_b32_e32 v22, 16, v22
	v_lshrrev_b32_e32 v23, 16, v23
	v_lshrrev_b32_e32 v25, 16, v25
	v_bfe_u32 v40, v24, 16, 1
	v_and_or_b32 v25, v34, s38, v25
	v_and_or_b32 v23, v37, s38, v23
	v_and_or_b32 v22, v36, s38, v22
	v_mul_f32_e32 v34, v66, v59
	v_and_b32_e32 v37, 0xffff0000, v27
	v_and_b32_e32 v36, 0xffff0000, v26
	v_add3_u32 v24, v24, v40, s39
	v_pk_mul_f32 v[36:37], v[34:35], v[36:37] op_sel_hi:[0,1]
	v_and_b32_e32 v39, 0xffff0000, v29
	v_and_b32_e32 v38, 0xffff0000, v28
	v_lshlrev_b32_e32 v29, 16, v29
	v_lshlrev_b32_e32 v28, 16, v28
	v_lshrrev_b32_e32 v24, 16, v24
	v_lshlrev_b32_e32 v27, 16, v27
	v_lshlrev_b32_e32 v26, 16, v26
	v_pk_mul_f32 v[38:39], v[34:35], v[38:39] op_sel_hi:[0,1]
	v_pk_mul_f32 v[28:29], v[34:35], v[28:29] op_sel_hi:[0,1]
	v_bfe_u32 v41, v37, 16, 1
	v_and_or_b32 v24, v35, s38, v24
	v_pk_mul_f32 v[26:27], v[34:35], v[26:27] op_sel_hi:[0,1]
	v_bfe_u32 v35, v39, 16, 1
	v_bfe_u32 v40, v38, 16, 1
	v_add3_u32 v37, v37, v41, s39
	v_bfe_u32 v41, v28, 16, 1
	v_bfe_u32 v59, v36, 16, 1
	v_add3_u32 v38, v38, v40, s39
	v_add3_u32 v35, v39, v35, s39
	v_bfe_u32 v39, v26, 16, 1
	v_bfe_u32 v40, v27, 16, 1
	v_add3_u32 v28, v28, v41, s39
	v_add3_u32 v36, v36, v59, s39
	v_bfe_u32 v59, v29, 16, 1
	v_add3_u32 v27, v27, v40, s39
	v_add3_u32 v26, v26, v39, s39
	v_lshrrev_b32_e32 v28, 16, v28
	v_add3_u32 v29, v29, v59, s39
	v_lshrrev_b32_e32 v26, 16, v26
	v_lshrrev_b32_e32 v27, 16, v27
	v_and_or_b32 v28, v38, s38, v28
	v_and_b32_e32 v39, 0xffff0000, v33
	v_and_b32_e32 v38, 0xffff0000, v32
	v_lshrrev_b32_e32 v29, 16, v29
	v_and_or_b32 v27, v37, s38, v27
	v_and_or_b32 v26, v36, s38, v26
	v_and_b32_e32 v37, 0xffff0000, v31
	v_and_b32_e32 v36, 0xffff0000, v30
	v_lshlrev_b32_e32 v31, 16, v31
	v_lshlrev_b32_e32 v30, 16, v30
	v_pk_mul_f32 v[38:39], v[34:35], v[38:39] op_sel_hi:[0,1]
	v_lshlrev_b32_e32 v33, 16, v33
	v_lshlrev_b32_e32 v32, 16, v32
	v_and_or_b32 v29, v35, s38, v29
	v_pk_mul_f32 v[36:37], v[34:35], v[36:37] op_sel_hi:[0,1]
	v_pk_mul_f32 v[30:31], v[34:35], v[30:31] op_sel_hi:[0,1]
	v_pk_mul_f32 v[32:33], v[34:35], v[32:33] op_sel_hi:[0,1]
	v_bfe_u32 v34, v39, 16, 1
	v_bfe_u32 v35, v38, 16, 1
	v_add3_u32 v35, v38, v35, s39
	v_add3_u32 v34, v39, v34, s39
	v_bfe_u32 v38, v30, 16, 1
	v_bfe_u32 v39, v31, 16, 1
	v_add3_u32 v31, v31, v39, s39
	v_add3_u32 v30, v30, v38, s39
	v_and_b32_e32 v38, -16, v42
	v_lshlrev_b32_e32 v39, 4, v232
	v_bfe_u32 v41, v36, 16, 1
	s_add_i32 s12, s50, -1
	v_bitop3_b32 v61, v39, v38, s0 bitop3:0x6c
	v_add_u32_e32 v38, 64, v38
	v_add3_u32 v36, v36, v41, s39
	v_bfe_u32 v41, v33, 16, 1
	v_bitop3_b32 v38, v39, v38, s0 bitop3:0x6c
	s_lshl_b32 s0, s12, 5
	v_add3_u32 v33, v33, v41, s39
	v_lshlrev_b32_e32 v59, 7, v232
	v_ashrrev_i32_e32 v41, 2, v42
	s_add_i32 s0, s0, s30
	v_bfe_u32 v40, v37, 16, 1
	v_and_b32_e32 v60, -4, v41
	v_add3_u32 v41, v38, v59, s1
	v_add3_u32 v59, v61, v59, s1
	s_ashr_i32 s1, s0, 31
	v_add3_u32 v37, v37, v40, s39
	v_bfe_u32 v40, v32, 16, 1
	s_lshl_b64 s[0:1], s[0:1], 9
	v_add3_u32 v32, v32, v40, s39
	v_lshrrev_b32_e32 v30, 16, v30
	v_lshrrev_b32_e32 v31, 16, v31
	s_add_u32 s0, s4, s0
	v_lshrrev_b32_e32 v32, 16, v32
	v_lshrrev_b32_e32 v33, 16, v33
	v_and_or_b32 v31, v37, s38, v31
	v_and_or_b32 v30, v36, s38, v30
	v_lshlrev_b64 v[36:37], 3, v[42:43]
	s_addc_u32 s1, s5, s1
	v_and_or_b32 v33, v34, s38, v33
	v_and_or_b32 v32, v35, s38, v32
	v_lshl_add_u64 v[34:35], s[4:5], 0, v[36:37]
	v_lshl_add_u64 v[36:37], s[0:1], 0, v[36:37]
	s_lshl_b32 s0, s50, 7
	v_readlane_b32 s1, v254, 10
	s_add_i32 s0, s1, s0
	s_cmp_ge_u32 s96, 4
	s_cbranch_scc0 .Lprio_p1_1
	s_setprio 1
.Lprio_p1_1:
	v_lshl_add_u32 v40, v0, 10, 0
	v_add_u32_e32 v60, s0, v60
	s_mov_b32 s0, 0
	s_waitcnt vmcnt(0)
	s_branch .LBB0_500
